# v40 + P2a accumulator zero-init moved from behind the prologue barrier into the W-load wait shadow
# baseline (speedup 1.0000x reference)
.LBB0_263:
	s_sub_i32 s7, s62, s64
	v_mov_b32_e32 v162, v0
	s_min_i32 s7, s7, 0x200
	s_add_i32 s8, s7, 0x7f
	v_readfirstlane_b32 s6, v162
	s_lshr_b32 s66, s8, 7
	s_ashr_i32 s8, s6, 2
	s_and_b32 s8, s8, -16
	s_mul_i32 s8, s8, s66
	s_add_i32 s8, s8, s64
	v_bfe_u32 v2, v162, 3, 3
	v_or_b32_e32 v10, s8, v2
	s_add_i32 s65, s7, s64
	v_mov_b32_e32 v11, s64
	v_cmp_gt_i32_e32 vcc, s65, v10
	v_or_b32_e32 v4, 8, v10
	v_add_u32_e32 v6, 16, v10
	v_cndmask_b32_e32 v2, v11, v10, vcc
	v_cmp_gt_i32_e32 vcc, s65, v4
	s_cmpk_gt_u32 s7, 0x80
	s_cselect_b64 s[46:47], -1, 0
	v_cndmask_b32_e32 v4, v11, v4, vcc
	v_cmp_gt_i32_e32 vcc, s65, v6
	s_and_b64 vcc, s[46:47], vcc
	v_add_u32_e32 v8, 24, v10
	v_cndmask_b32_e32 v6, v11, v6, vcc
	v_cmp_gt_i32_e32 vcc, s65, v8
	s_and_b64 vcc, s[46:47], vcc
	v_ashrrev_i32_e32 v3, 31, v2
	v_ashrrev_i32_e32 v7, 31, v6
	v_cndmask_b32_e32 v8, v11, v8, vcc
	v_lshl_add_u64 v[2:3], v[2:3], 2, s[24:25]
	v_ashrrev_i32_e32 v5, 31, v4
	v_lshl_add_u64 v[6:7], v[6:7], 2, s[24:25]
	v_ashrrev_i32_e32 v9, 31, v8
	v_lshl_add_u64 v[4:5], v[4:5], 2, s[24:25]
	v_lshl_add_u64 v[8:9], v[8:9], 2, s[24:25]
	global_load_dword v12, v[2:3], off
	global_load_dword v13, v[4:5], off
	s_nop 0
	global_load_dword v6, v[6:7], off
	s_nop 0
	global_load_dword v7, v[8:9], off
	v_add_u32_e32 v2, 32, v10
	s_cmpk_gt_u32 s7, 0x100
	s_cselect_b64 s[44:45], -1, 0
	v_cmp_gt_i32_e32 vcc, s65, v2
	s_and_b64 vcc, s[44:45], vcc
	v_add_u32_e32 v4, 40, v10
	v_cndmask_b32_e32 v2, v11, v2, vcc
	v_cmp_gt_i32_e32 vcc, s65, v4
	s_and_b64 vcc, s[44:45], vcc
	v_ashrrev_i32_e32 v3, 31, v2
	v_cndmask_b32_e32 v4, v11, v4, vcc
	v_lshl_add_u64 v[2:3], v[2:3], 2, s[24:25]
	v_ashrrev_i32_e32 v5, 31, v4
	v_lshl_add_u64 v[4:5], v[4:5], 2, s[24:25]
	global_load_dword v8, v[2:3], off
	global_load_dword v9, v[4:5], off
	v_add_u32_e32 v2, 48, v10
	s_cmpk_gt_u32 s7, 0x180
	s_cselect_b64 s[42:43], -1, 0
	v_cmp_gt_i32_e32 vcc, s65, v2
	s_and_b64 vcc, s[42:43], vcc
	v_add_u32_e32 v4, 56, v10
	v_cndmask_b32_e32 v2, v11, v2, vcc
	v_cmp_gt_i32_e32 vcc, s65, v4
	s_and_b64 vcc, s[42:43], vcc
	v_ashrrev_i32_e32 v3, 31, v2
	v_cndmask_b32_e32 v4, v11, v4, vcc
	v_lshl_add_u64 v[2:3], v[2:3], 2, s[24:25]
	v_ashrrev_i32_e32 v5, 31, v4
	v_lshl_add_u64 v[4:5], v[4:5], 2, s[24:25]
	global_load_dword v131, v[2:3], off
	global_load_dword v130, v[4:5], off
	v_and_b32_e32 v10, 31, v162
	v_and_b32_e32 v2, 7, v162
	v_bfe_u32 v3, v162, 4, 2
	v_cmp_gt_u32_e32 vcc, 16, v10
	v_bitop3_b32 v2, v3, v2, 4 bitop3:0x36
	v_ashrrev_i32_e32 v11, 5, v162
	v_cndmask_b32_e32 v15, v166, v167, vcc
	v_bitop3_b32 v14, v3, v162, 7 bitop3:0x78
	v_lshlrev_b32_e32 v132, 4, v2
	v_lshl_add_u32 v2, v10, 4, v15
	v_lshlrev_b32_e32 v133, 4, v14
	v_lshl_or_b32 v168, v11, 13, v2
	global_load_dwordx4 v[228:231], v168, s[22:23]
	global_load_dwordx4 v[232:235], v168, s[22:23] offset:2048
	global_load_dwordx4 v[236:239], v168, s[28:29]
	global_load_dwordx4 v[240:243], v168, s[28:29] offset:2048
	global_load_dwordx4 v[60:63], v168, s[30:31]
	global_load_dwordx4 v[64:67], v168, s[30:31] offset:2048
	global_load_dwordx4 v[68:71], v168, s[34:35]
	global_load_dwordx4 v[72:75], v168, s[34:35] offset:2048
	v_lshrrev_b32_e32 v5, 4, v162
	v_lshlrev_b32_e32 v3, 11, v3
	s_lshl_b32 s6, s6, 8
	s_and_b32 s6, s6, 0xffffc000
	v_and_b32_e32 v4, 15, v162
	s_add_i32 s67, s6, 0
	s_add_i32 s68, s67, 0x400
	s_mov_b64 s[6:7], -1
	s_mov_b64 s[8:9], 0
	s_cmp_lt_i32 s66, 2
	s_mov_b64 s[10:11], 0
	s_waitcnt vmcnt(15)
	v_lshlrev_b32_e32 v2, 8, v12
	v_and_or_b32 v169, v2, s60, v133
	s_waitcnt vmcnt(14)
	v_lshlrev_b32_e32 v2, 8, v13
	v_and_or_b32 v170, v2, s60, v132
	s_waitcnt vmcnt(13)
	v_lshlrev_b32_e32 v2, 8, v6
	s_waitcnt vmcnt(12)
	v_lshlrev_b32_e32 v6, 8, v7
	v_and_or_b32 v175, v6, s60, v132
	v_and_or_b32 v174, v2, s60, v133
	s_waitcnt vmcnt(11)
	v_lshlrev_b32_e32 v2, 8, v8
	s_waitcnt vmcnt(10)
	v_lshlrev_b32_e32 v6, 8, v9
	v_and_or_b32 v177, v6, s60, v132
	v_lshlrev_b32_e32 v6, 3, v162
	v_and_or_b32 v176, v2, s60, v133
	v_lshlrev_b32_e32 v2, 10, v11
	v_and_b32_e32 v6, 24, v6
	v_add3_u32 v173, s61, v2, v6
	v_bfe_u32 v2, v162, 2, 3
	v_bitop3_b32 v134, v2, v5, 4 bitop3:0x78
	v_bfe_u32 v2, v162, 2, 2
	v_lshlrev_b32_e32 v7, 8, v2
	v_add3_u32 v3, s61, v3, v7
	v_lshrrev_b32_e32 v7, 2, v162
	v_and_or_b32 v2, v7, 4, v2
	v_lshlrev_b32_e32 v2, 5, v2
	v_add3_u32 v171, v3, v6, v2
	v_bfe_u32 v3, v162, 1, 3
	v_bitop3_b32 v3, v5, v3, 3 bitop3:0x6c
	v_lshlrev_b32_e32 v2, 7, v4
	v_lshlrev_b32_e32 v3, 4, v3
	v_add3_u32 v172, s67, v2, v3
	s_cbranch_scc1 .LBB0_275
	s_cmp_gt_i32 s66, 2
	s_cbranch_scc0 .LBB0_269
	s_cmp_eq_u32 s66, 3
	s_mov_b64 s[10:11], -1
	s_cbranch_scc0 .LBB0_270
	s_mov_b32 s6, m0
	s_mov_b32 m0, s67
	s_nop 0
	global_load_lds_dwordx4 v169, s[18:19]
	s_mov_b32 m0, s6
	s_add_i32 s52, s67, 0x800
	s_mov_b32 s6, m0
	s_mov_b32 m0, s68
	s_nop 0
	global_load_lds_dwordx4 v170, s[18:19]
	s_mov_b32 m0, s6
	s_add_i32 s53, s67, 0xc00
	s_mov_b32 s6, m0
	s_mov_b32 m0, s52
	s_nop 0
	global_load_lds_dwordx4 v174, s[18:19]
	s_mov_b32 m0, s6
	s_add_i32 s69, s67, 0x1000
	s_mov_b32 s6, m0
	s_mov_b32 m0, s53
	s_nop 0
	global_load_lds_dwordx4 v175, s[18:19]
	s_mov_b32 m0, s6
	s_add_i32 s70, s67, 0x1400
	s_mov_b32 s6, m0
	s_mov_b32 m0, s69
	s_nop 0
	global_load_lds_dwordx4 v176, s[18:19]
	s_mov_b32 m0, s6
	v_mov_b32_e32 v26, 0
	s_mov_b32 s6, m0
	s_mov_b32 m0, s70
	s_nop 0
	global_load_lds_dwordx4 v177, s[18:19]
	s_mov_b32 m0, s6
	v_mov_b32_e32 v27, 0
	v_mov_b32_e32 v28, 0
	v_mov_b32_e32 v29, 0
	v_mov_b32_e32 v10, 0
	v_mov_b32_e32 v11, 0
	v_mov_b32_e32 v12, 0
	v_mov_b32_e32 v13, 0
	v_mov_b32_e32 v50, 0
	v_mov_b32_e32 v51, 0
	v_mov_b32_e32 v52, 0
	v_mov_b32_e32 v53, 0
	v_mov_b32_e32 v14, 0
	v_mov_b32_e32 v15, 0
	v_mov_b32_e32 v16, 0
	v_mov_b32_e32 v17, 0
	v_mov_b32_e32 v30, 0
	v_mov_b32_e32 v31, 0
	v_mov_b32_e32 v32, 0
	v_mov_b32_e32 v33, 0
	v_mov_b32_e32 v34, 0
	v_mov_b32_e32 v35, 0
	v_mov_b32_e32 v36, 0
	v_mov_b32_e32 v37, 0
	v_mov_b32_e32 v82, 0
	v_mov_b32_e32 v83, 0
	v_mov_b32_e32 v84, 0
	v_mov_b32_e32 v85, 0
	v_mov_b32_e32 v54, 0
	v_mov_b32_e32 v55, 0
	v_mov_b32_e32 v56, 0
	v_mov_b32_e32 v57, 0
	v_mov_b32_e32 v86, 0
	v_mov_b32_e32 v87, 0
	v_mov_b32_e32 v88, 0
	v_mov_b32_e32 v89, 0
	v_mov_b32_e32 v22, 0
	v_mov_b32_e32 v23, 0
	v_mov_b32_e32 v24, 0
	v_mov_b32_e32 v25, 0
	v_mov_b32_e32 v6, 0
	v_mov_b32_e32 v7, 0
	v_mov_b32_e32 v8, 0
	v_mov_b32_e32 v9, 0
	v_mov_b32_e32 v42, 0
	v_mov_b32_e32 v43, 0
	v_mov_b32_e32 v44, 0
	v_mov_b32_e32 v45, 0
	v_mov_b32_e32 v38, 0
	v_mov_b32_e32 v39, 0
	v_mov_b32_e32 v40, 0
	v_mov_b32_e32 v41, 0
	v_mov_b32_e32 v18, 0
	v_mov_b32_e32 v19, 0
	v_mov_b32_e32 v20, 0
	v_mov_b32_e32 v21, 0
	v_mov_b32_e32 v58, 0
	v_mov_b32_e32 v59, 0
	v_mov_b32_e32 v46, 0
	v_mov_b32_e32 v47, 0
	v_mov_b32_e32 v48, 0
	v_mov_b32_e32 v49, 0
	v_mov_b32_e32 v90, 0
	v_mov_b32_e32 v91, 0
	v_mov_b32_e32 v92, 0
	v_mov_b32_e32 v93, 0
	v_mov_b32_e32 v78, 0
	v_mov_b32_e32 v79, 0
	v_mov_b32_e32 v80, 0
	v_mov_b32_e32 v81, 0
	v_mov_b32_e32 v76, 0
	v_mov_b32_e32 v77, 0
	v_mov_b32_e32 v94, 0
	v_mov_b32_e32 v95, 0
	v_mov_b32_e32 v96, 0
	v_mov_b32_e32 v97, 0
	s_waitcnt vmcnt(6)
	v_mov_b32_e32 v106, v60
	v_mov_b32_e32 v107, v61
	v_mov_b32_e32 v108, v62
	v_mov_b32_e32 v109, v63
	v_mov_b32_e32 v102, v64
	v_mov_b32_e32 v103, v65
	v_mov_b32_e32 v104, v66
	v_mov_b32_e32 v105, v67
	v_mov_b32_e32 v110, v68
	v_mov_b32_e32 v111, v69
	v_mov_b32_e32 v112, v70
	v_mov_b32_e32 v113, v71
	v_mov_b32_e32 v98, v72
	v_mov_b32_e32 v99, v73
	v_mov_b32_e32 v100, v74
	v_mov_b32_e32 v101, v75
	v_xor_b32_e32 v139, 64, v172
	v_cvt_pk_bf16_f32 v2, v228, v229
	v_cvt_pk_bf16_f32 v3, v230, v231
	v_lshlrev_b32_e32 v4, 5, v134
	v_add_u32_e32 v135, v173, v4
	v_xor_b32_e32 v5, 32, v4
	ds_write_b64 v135, v[2:3]
	v_cvt_pk_bf16_f32 v2, v232, v233
	v_cvt_pk_bf16_f32 v3, v234, v235
	v_add_u32_e32 v136, v173, v5
	v_xor_b32_e32 v5, 64, v4
	ds_write_b64 v136, v[2:3] offset:256
	v_cvt_pk_bf16_f32 v2, v236, v237
	v_cvt_pk_bf16_f32 v3, v238, v239
	v_add_u32_e32 v137, v173, v5
	v_xor_b32_e32 v4, 0x60, v4
	ds_write_b64 v137, v[2:3] offset:512
	v_cvt_pk_bf16_f32 v2, v240, v241
	v_cvt_pk_bf16_f32 v3, v242, v243
	v_add_u32_e32 v138, v173, v4
	ds_write_b64 v138, v[2:3] offset:768
	global_load_dwordx4 v[122:125], v168, s[38:39]
	global_load_dwordx4 v[118:121], v168, s[38:39] offset:2048
	global_load_dwordx4 v[126:129], v168, s[40:41]
	global_load_dwordx4 v[114:117], v168, s[40:41] offset:2048
	s_waitcnt lgkmcnt(0)
	s_barrier
	v_add_u32_e32 v2, 0x2000, v172
	s_add_i32 s71, s67, 0x2000
	v_xor_b32_e32 v140, 64, v2
	v_xor_b32_e32 v141, 32, v171
	v_xor_b32_e32 v142, 64, v171
	v_xor_b32_e32 v143, 0x60, v171
	v_xor_b32_e32 v144, 0x80, v171
	v_xor_b32_e32 v145, 0xa0, v171
	v_xor_b32_e32 v146, 0xc0, v171
	s_add_i32 s72, s67, 0x2400
	v_xor_b32_e32 v147, 0xe0, v171
	s_add_i32 s73, s67, 0x2800
	s_add_i32 s74, s67, 0x2c00
	s_add_i32 s75, s67, 0x3000
	s_add_i32 s76, s67, 0x3400
	s_mov_b32 s50, 0
	s_mov_b64 s[10:11], 0
	v_mov_b32_e32 v2, v26
	v_mov_b32_e32 v3, v26
	v_mov_b32_e32 v4, v26
	v_mov_b32_e32 v5, v26
	v_mov_b32_e32 v66, v26
	v_mov_b32_e32 v67, v26
	v_mov_b32_e32 v68, v26
	v_mov_b32_e32 v69, v26
	v_mov_b32_e32 v62, v26
	v_mov_b32_e32 v63, v26
	v_mov_b32_e32 v64, v26
	v_mov_b32_e32 v65, v26
	v_mov_b32_e32 v70, v26
	v_mov_b32_e32 v71, v26
	v_mov_b32_e32 v72, v26
	v_mov_b32_e32 v73, v26
	v_mov_b32_e32 v60, v26
	v_mov_b32_e32 v61, v26
	v_mov_b32_e32 v74, v26
	v_mov_b32_e32 v75, v26

.LBB0_271:
	s_mov_b32 s6, m0
	s_mov_b32 m0, s67
	s_nop 0
	global_load_lds_dwordx4 v169, s[18:19]
	s_mov_b32 m0, s6
	s_add_i32 s69, s67, 0x800
	s_mov_b32 s6, m0
	s_mov_b32 m0, s68
	s_nop 0
	global_load_lds_dwordx4 v170, s[18:19]
	s_mov_b32 m0, s6
	s_add_i32 s70, s67, 0xc00
	s_mov_b32 s6, m0
	s_mov_b32 m0, s69
	s_nop 0
	global_load_lds_dwordx4 v174, s[18:19]
	s_mov_b32 m0, s6
	v_xor_b32_e32 v102, 64, v172
	s_mov_b32 s6, m0
	s_mov_b32 m0, s70
	s_nop 0
	global_load_lds_dwordx4 v175, s[18:19]
	s_mov_b32 m0, s6
	v_mov_b32_e32 v10, 0
	v_mov_b32_e32 v11, 0
	v_mov_b32_e32 v12, 0
	v_mov_b32_e32 v13, 0
	v_mov_b32_e32 v14, 0
	v_mov_b32_e32 v15, 0
	v_mov_b32_e32 v16, 0
	v_mov_b32_e32 v17, 0
	v_mov_b32_e32 v30, 0
	v_mov_b32_e32 v31, 0
	v_mov_b32_e32 v32, 0
	v_mov_b32_e32 v33, 0
	v_mov_b32_e32 v34, 0
	v_mov_b32_e32 v35, 0
	v_mov_b32_e32 v36, 0
	v_mov_b32_e32 v37, 0
	v_mov_b32_e32 v54, 0
	v_mov_b32_e32 v55, 0
	v_mov_b32_e32 v56, 0
	v_mov_b32_e32 v57, 0
	v_mov_b32_e32 v86, 0
	v_mov_b32_e32 v87, 0
	v_mov_b32_e32 v88, 0
	v_mov_b32_e32 v89, 0
	v_mov_b32_e32 v6, 0
	v_mov_b32_e32 v7, 0
	v_mov_b32_e32 v8, 0
	v_mov_b32_e32 v9, 0
	v_mov_b32_e32 v42, 0
	v_mov_b32_e32 v43, 0
	v_mov_b32_e32 v44, 0
	v_mov_b32_e32 v45, 0
	v_mov_b32_e32 v18, 0
	v_mov_b32_e32 v19, 0
	v_mov_b32_e32 v20, 0
	v_mov_b32_e32 v21, 0
	v_mov_b32_e32 v46, 0
	v_mov_b32_e32 v47, 0
	v_mov_b32_e32 v48, 0
	v_mov_b32_e32 v49, 0
	v_mov_b32_e32 v90, 0
	v_mov_b32_e32 v91, 0
	v_mov_b32_e32 v92, 0
	v_mov_b32_e32 v93, 0
	v_mov_b32_e32 v76, 0
	v_mov_b32_e32 v77, 0
	v_mov_b32_e32 v94, 0
	v_mov_b32_e32 v95, 0
	v_mov_b32_e32 v96, 0
	v_mov_b32_e32 v97, 0
	s_waitcnt vmcnt(4)
	v_mov_b32_e32 v38, v60
	v_mov_b32_e32 v39, v61
	v_mov_b32_e32 v40, v62
	v_mov_b32_e32 v41, v63
	v_mov_b32_e32 v26, v64
	v_mov_b32_e32 v27, v65
	v_mov_b32_e32 v28, v66
	v_mov_b32_e32 v29, v67
	v_mov_b32_e32 v50, v68
	v_mov_b32_e32 v51, v69
	v_mov_b32_e32 v52, v70
	v_mov_b32_e32 v53, v71
	v_mov_b32_e32 v22, v72
	v_mov_b32_e32 v23, v73
	v_mov_b32_e32 v24, v74
	v_mov_b32_e32 v25, v75
	s_add_i32 s71, s67, 0x2000
	v_cvt_pk_bf16_f32 v2, v228, v229
	v_cvt_pk_bf16_f32 v3, v230, v231
	v_lshlrev_b32_e32 v4, 5, v134
	v_add_u32_e32 v98, v173, v4
	v_xor_b32_e32 v5, 32, v4
	ds_write_b64 v98, v[2:3]
	v_cvt_pk_bf16_f32 v2, v232, v233
	v_cvt_pk_bf16_f32 v3, v234, v235
	v_add_u32_e32 v99, v173, v5
	v_xor_b32_e32 v5, 64, v4
	ds_write_b64 v99, v[2:3] offset:256
	v_cvt_pk_bf16_f32 v2, v236, v237
	v_cvt_pk_bf16_f32 v3, v238, v239
	v_add_u32_e32 v100, v173, v5
	v_xor_b32_e32 v4, 0x60, v4
	ds_write_b64 v100, v[2:3] offset:512
	v_cvt_pk_bf16_f32 v2, v240, v241
	v_cvt_pk_bf16_f32 v3, v242, v243
	v_add_u32_e32 v101, v173, v4
	ds_write_b64 v101, v[2:3] offset:768
	global_load_dwordx4 v[78:81], v168, s[38:39]
	global_load_dwordx4 v[66:69], v168, s[38:39] offset:2048
	global_load_dwordx4 v[82:85], v168, s[40:41]
	global_load_dwordx4 v[58:61], v168, s[40:41] offset:2048
	s_waitcnt lgkmcnt(0)
	s_barrier
	v_add_u32_e32 v2, 0x2000, v172
	v_xor_b32_e32 v103, 64, v2
	v_mov_b32_e32 v2, 0
	v_xor_b32_e32 v104, 32, v171
	v_xor_b32_e32 v105, 64, v171
	v_xor_b32_e32 v106, 0x60, v171
	v_xor_b32_e32 v107, 0x80, v171
	v_xor_b32_e32 v108, 0xa0, v171
	v_xor_b32_e32 v109, 0xc0, v171
	s_add_i32 s72, s67, 0x2400
	v_xor_b32_e32 v110, 0xe0, v171
	s_add_i32 s73, s67, 0x2800
	s_add_i32 s74, s67, 0x2c00
	s_mov_b32 s52, 0
	s_mov_b64 s[48:49], 0
	v_mov_b32_e32 v3, v2
	v_mov_b32_e32 v4, v2
	v_mov_b32_e32 v5, v2
	v_mov_b32_e32 v62, v2
	v_mov_b32_e32 v63, v2
	v_mov_b32_e32 v64, v2
	v_mov_b32_e32 v65, v2
	v_mov_b32_e32 v70, v2
	v_mov_b32_e32 v71, v2
	v_mov_b32_e32 v72, v2
	v_mov_b32_e32 v73, v2
	v_mov_b32_e32 v74, v2
	v_mov_b32_e32 v75, v2

.LBB0_277:
	v_mov_b32_e32 v125, 0
	v_lshlrev_b32_e32 v98, 5, v134
	v_add_u32_e32 v99, 0x2000, v172
	s_andn2_b64 vcc, exec, s[10:11]
	v_xor_b32_e32 v178, 64, v172
	v_xor_b32_e32 v179, 32, v171
	v_xor_b32_e32 v180, 64, v171
	v_xor_b32_e32 v181, 0x60, v171
	v_xor_b32_e32 v182, 0x80, v171
	v_xor_b32_e32 v183, 0xa0, v171
	v_xor_b32_e32 v184, 0xc0, v171
	v_xor_b32_e32 v185, 0xe0, v171
	v_add_u32_e32 v186, v173, v98
	v_xor_b32_e32 v190, 32, v98
	v_xor_b32_e32 v189, 64, v98
	v_xor_b32_e32 v188, 0x60, v98
	v_xor_b32_e32 v187, 64, v99
	v_mov_b32_e32 v124, v125
	v_mov_b32_e32 v123, v125
	v_mov_b32_e32 v122, v125
	v_mov_b32_e32 v117, v125
	v_mov_b32_e32 v116, v125
	v_mov_b32_e32 v115, v125
	v_mov_b32_e32 v114, v125
	v_mov_b32_e32 v109, v125
	v_mov_b32_e32 v108, v125
	v_mov_b32_e32 v107, v125
	v_mov_b32_e32 v106, v125
	v_mov_b32_e32 v105, v125
	v_mov_b32_e32 v104, v125
	v_mov_b32_e32 v103, v125
	v_mov_b32_e32 v102, v125
	v_mov_b32_e32 v129, v125
	v_mov_b32_e32 v128, v125
	v_mov_b32_e32 v127, v125
	v_mov_b32_e32 v126, v125
	v_mov_b32_e32 v121, v125
	v_mov_b32_e32 v120, v125
	v_mov_b32_e32 v119, v125
	v_mov_b32_e32 v118, v125
	v_mov_b32_e32 v113, v125
	v_mov_b32_e32 v112, v125
	v_mov_b32_e32 v111, v125
	v_mov_b32_e32 v110, v125
	v_mov_b32_e32 v101, v125
	v_mov_b32_e32 v100, v125
	v_mov_b32_e32 v99, v125
	v_mov_b32_e32 v98, v125
	s_cbranch_vccnz .LBB0_281
	s_waitcnt vmcnt(9)
	v_lshlrev_b32_e32 v2, 8, v131
	v_and_or_b32 v191, v2, s60, v133
	s_waitcnt vmcnt(8)
	v_lshlrev_b32_e32 v2, 8, v130
	v_and_or_b32 v192, v2, s60, v132
	s_mov_b32 s6, m0
	s_mov_b32 m0, s67
	s_nop 0
	global_load_lds_dwordx4 v169, s[18:19]
	s_mov_b32 m0, s6
	s_add_i32 s50, s67, 0x800
	s_mov_b32 s6, m0
	s_mov_b32 m0, s68
	s_nop 0
	global_load_lds_dwordx4 v170, s[18:19]
	s_mov_b32 m0, s6
	s_add_i32 s51, s67, 0xc00
	s_mov_b32 s6, m0
	s_mov_b32 m0, s50
	s_nop 0
	global_load_lds_dwordx4 v174, s[18:19]
	s_mov_b32 m0, s6
	s_add_i32 s52, s67, 0x1000
	s_mov_b32 s6, m0
	s_mov_b32 m0, s51
	s_nop 0
	global_load_lds_dwordx4 v175, s[18:19]
	s_mov_b32 m0, s6
	s_add_i32 s53, s67, 0x1400
	s_mov_b32 s6, m0
	s_mov_b32 m0, s52
	s_nop 0
	global_load_lds_dwordx4 v176, s[18:19]
	s_mov_b32 m0, s6
	s_add_i32 s69, s67, 0x1800
	s_mov_b32 s6, m0
	s_mov_b32 m0, s53
	s_nop 0
	global_load_lds_dwordx4 v177, s[18:19]
	s_mov_b32 m0, s6
	s_add_i32 s70, s67, 0x1c00
	s_mov_b32 s6, m0
	s_mov_b32 m0, s69
	s_nop 0
	global_load_lds_dwordx4 v191, s[18:19]
	s_mov_b32 m0, s6
	v_add_u32_e32 v193, v173, v190
	s_mov_b32 s6, m0
	s_mov_b32 m0, s70
	s_nop 0
	global_load_lds_dwordx4 v192, s[18:19]
	s_mov_b32 m0, s6
	v_mov_b32_e32 v99, 0
	v_mov_b32_e32 v100, 0
	v_mov_b32_e32 v101, 0
	v_mov_b32_e32 v26, 0
	v_mov_b32_e32 v27, 0
	v_mov_b32_e32 v28, 0
	v_mov_b32_e32 v29, 0
	v_mov_b32_e32 v4, 0
	v_mov_b32_e32 v5, 0
	v_mov_b32_e32 v10, 0
	v_mov_b32_e32 v11, 0
	v_mov_b32_e32 v12, 0
	v_mov_b32_e32 v13, 0
	v_mov_b32_e32 v110, 0
	v_mov_b32_e32 v111, 0
	v_mov_b32_e32 v112, 0
	v_mov_b32_e32 v113, 0
	v_mov_b32_e32 v50, 0
	v_mov_b32_e32 v51, 0
	v_mov_b32_e32 v52, 0
	v_mov_b32_e32 v53, 0
	v_mov_b32_e32 v14, 0
	v_mov_b32_e32 v15, 0
	v_mov_b32_e32 v16, 0
	v_mov_b32_e32 v17, 0
	v_mov_b32_e32 v30, 0
	v_mov_b32_e32 v31, 0
	v_mov_b32_e32 v32, 0
	v_mov_b32_e32 v33, 0
	v_mov_b32_e32 v118, 0
	v_mov_b32_e32 v119, 0
	v_mov_b32_e32 v120, 0
	v_mov_b32_e32 v121, 0
	v_mov_b32_e32 v34, 0
	v_mov_b32_e32 v35, 0
	v_mov_b32_e32 v36, 0
	v_mov_b32_e32 v37, 0
	v_mov_b32_e32 v126, 0
	v_mov_b32_e32 v127, 0
	v_mov_b32_e32 v128, 0
	v_mov_b32_e32 v129, 0
	v_mov_b32_e32 v82, 0
	v_mov_b32_e32 v83, 0
	v_mov_b32_e32 v84, 0
	v_mov_b32_e32 v85, 0
	v_mov_b32_e32 v54, 0
	v_mov_b32_e32 v55, 0
	v_mov_b32_e32 v56, 0
	v_mov_b32_e32 v57, 0
	v_mov_b32_e32 v86, 0
	v_mov_b32_e32 v87, 0
	v_mov_b32_e32 v88, 0
	v_mov_b32_e32 v89, 0
	v_mov_b32_e32 v102, 0
	v_mov_b32_e32 v103, 0
	v_mov_b32_e32 v104, 0
	v_mov_b32_e32 v105, 0
	v_mov_b32_e32 v22, 0
	v_mov_b32_e32 v23, 0
	v_mov_b32_e32 v24, 0
	v_mov_b32_e32 v25, 0
	v_mov_b32_e32 v6, 0
	v_mov_b32_e32 v7, 0
	v_mov_b32_e32 v8, 0
	v_mov_b32_e32 v9, 0
	v_mov_b32_e32 v42, 0
	v_mov_b32_e32 v43, 0
	v_mov_b32_e32 v44, 0
	v_mov_b32_e32 v45, 0
	v_mov_b32_e32 v106, 0
	v_mov_b32_e32 v107, 0
	v_mov_b32_e32 v108, 0
	v_mov_b32_e32 v109, 0
	v_mov_b32_e32 v38, 0
	v_mov_b32_e32 v39, 0
	v_mov_b32_e32 v40, 0
	v_mov_b32_e32 v41, 0
	v_mov_b32_e32 v18, 0
	v_mov_b32_e32 v19, 0
	v_mov_b32_e32 v20, 0
	v_mov_b32_e32 v21, 0
	v_mov_b32_e32 v114, 0
	v_mov_b32_e32 v115, 0
	v_mov_b32_e32 v116, 0
	v_mov_b32_e32 v117, 0
	v_mov_b32_e32 v58, 0
	v_mov_b32_e32 v59, 0
	v_mov_b32_e32 v46, 0
	v_mov_b32_e32 v47, 0
	v_mov_b32_e32 v48, 0
	v_mov_b32_e32 v49, 0
	v_mov_b32_e32 v90, 0
	v_mov_b32_e32 v91, 0
	v_mov_b32_e32 v92, 0
	v_mov_b32_e32 v93, 0
	v_mov_b32_e32 v122, 0
	v_mov_b32_e32 v123, 0
	v_mov_b32_e32 v124, 0
	v_mov_b32_e32 v125, 0
	v_mov_b32_e32 v78, 0
	v_mov_b32_e32 v79, 0
	v_mov_b32_e32 v80, 0
	v_mov_b32_e32 v81, 0
	v_mov_b32_e32 v76, 0
	v_mov_b32_e32 v77, 0
	v_mov_b32_e32 v94, 0
	v_mov_b32_e32 v95, 0
	v_mov_b32_e32 v96, 0
	v_mov_b32_e32 v97, 0
	s_waitcnt vmcnt(8)
	v_mov_b32_e32 v138, v60
	v_mov_b32_e32 v139, v61
	v_mov_b32_e32 v140, v62
	v_mov_b32_e32 v141, v63
	v_mov_b32_e32 v134, v64
	v_mov_b32_e32 v135, v65
	v_mov_b32_e32 v136, v66
	v_mov_b32_e32 v137, v67
	v_mov_b32_e32 v142, v68
	v_mov_b32_e32 v143, v69
	v_mov_b32_e32 v144, v70
	v_mov_b32_e32 v145, v71
	v_mov_b32_e32 v130, v72
	v_mov_b32_e32 v131, v73
	v_mov_b32_e32 v132, v74
	v_mov_b32_e32 v133, v75
	v_add_u32_e32 v194, v173, v189
	v_cvt_pk_bf16_f32 v2, v228, v229
	v_cvt_pk_bf16_f32 v3, v230, v231
	ds_write_b64 v186, v[2:3]
	v_cvt_pk_bf16_f32 v2, v232, v233
	v_cvt_pk_bf16_f32 v3, v234, v235
	ds_write_b64 v193, v[2:3] offset:256
	v_cvt_pk_bf16_f32 v2, v236, v237
	v_cvt_pk_bf16_f32 v3, v238, v239
	ds_write_b64 v194, v[2:3] offset:512
	v_cvt_pk_bf16_f32 v2, v240, v241
	v_cvt_pk_bf16_f32 v3, v242, v243
	v_add_u32_e32 v195, v173, v188
	ds_write_b64 v195, v[2:3] offset:768
	global_load_dwordx4 v[154:157], v168, s[38:39]
	global_load_dwordx4 v[150:153], v168, s[38:39] offset:2048
	global_load_dwordx4 v[158:161], v168, s[40:41]
	global_load_dwordx4 v[146:149], v168, s[40:41] offset:2048
	s_waitcnt lgkmcnt(0)
	s_barrier
	v_mov_b32_e32 v98, 0
	s_add_i32 s71, s67, 0x2000
	s_add_i32 s72, s67, 0x2400
	s_add_i32 s73, s67, 0x2800
	s_add_i32 s74, s67, 0x2c00
	s_add_i32 s75, s67, 0x3000
	s_add_i32 s76, s67, 0x3400
	s_add_i32 s77, s67, 0x3800
	s_add_i32 s78, s67, 0x3c00
	s_mov_b32 s48, 0
	s_mov_b64 s[8:9], 0
	v_mov_b32_e32 v2, v98
	v_mov_b32_e32 v3, v98
	v_mov_b32_e32 v66, v98
	v_mov_b32_e32 v67, v98
	v_mov_b32_e32 v68, v98
	v_mov_b32_e32 v69, v98
	v_mov_b32_e32 v62, v98
	v_mov_b32_e32 v63, v98
	v_mov_b32_e32 v64, v98
	v_mov_b32_e32 v65, v98
	v_mov_b32_e32 v70, v98
	v_mov_b32_e32 v71, v98
	v_mov_b32_e32 v72, v98
	v_mov_b32_e32 v73, v98
	v_mov_b32_e32 v60, v98
	v_mov_b32_e32 v61, v98
	v_mov_b32_e32 v74, v98
	v_mov_b32_e32 v75, v98

.LBB0_281:
	s_and_b64 vcc, exec, s[8:9]
	s_cbranch_vccz .LBB0_285
	s_mov_b32 s6, m0
	s_mov_b32 m0, s67
	s_nop 0
	global_load_lds_dwordx4 v169, s[18:19]
	s_mov_b32 m0, s6
	v_add_u32_e32 v47, v173, v189
	s_mov_b32 s6, m0
	s_mov_b32 m0, s68
	s_nop 0
	global_load_lds_dwordx4 v170, s[18:19]
	s_mov_b32 m0, s6
	v_mov_b32_e32 v30, 0
	v_mov_b32_e32 v31, 0
	v_mov_b32_e32 v32, 0
	v_mov_b32_e32 v33, 0
	v_mov_b32_e32 v86, 0
	v_mov_b32_e32 v87, 0
	v_mov_b32_e32 v88, 0
	v_mov_b32_e32 v89, 0
	v_mov_b32_e32 v42, 0
	v_mov_b32_e32 v43, 0
	v_mov_b32_e32 v44, 0
	v_mov_b32_e32 v45, 0
	v_mov_b32_e32 v90, 0
	v_mov_b32_e32 v91, 0
	v_mov_b32_e32 v92, 0
	v_mov_b32_e32 v93, 0
	v_mov_b32_e32 v94, 0
	v_mov_b32_e32 v95, 0
	v_mov_b32_e32 v96, 0
	v_mov_b32_e32 v97, 0
	s_waitcnt vmcnt(2)
	v_mov_b32_e32 v18, v60
	v_mov_b32_e32 v19, v61
	v_mov_b32_e32 v20, v62
	v_mov_b32_e32 v21, v63
	v_mov_b32_e32 v6, v64
	v_mov_b32_e32 v7, v65
	v_mov_b32_e32 v8, v66
	v_mov_b32_e32 v9, v67
	v_mov_b32_e32 v14, v68
	v_mov_b32_e32 v15, v69
	v_mov_b32_e32 v16, v70
	v_mov_b32_e32 v17, v71
	v_mov_b32_e32 v2, v72
	v_mov_b32_e32 v3, v73
	v_mov_b32_e32 v4, v74
	v_mov_b32_e32 v5, v75
	v_add_u32_e32 v46, v173, v190
	v_cvt_pk_bf16_f32 v10, v228, v229
	v_cvt_pk_bf16_f32 v11, v230, v231
	ds_write_b64 v186, v[10:11]
	v_cvt_pk_bf16_f32 v10, v236, v237
	v_cvt_pk_bf16_f32 v11, v238, v239
	v_cvt_pk_bf16_f32 v12, v232, v233
	v_cvt_pk_bf16_f32 v13, v234, v235
	ds_write_b64 v47, v[10:11] offset:512
	v_cvt_pk_bf16_f32 v10, v240, v241
	v_cvt_pk_bf16_f32 v11, v242, v243
	v_add_u32_e32 v48, v173, v188
	ds_write_b64 v46, v[12:13] offset:256
	ds_write_b64 v48, v[10:11] offset:768
	global_load_dwordx4 v[38:41], v168, s[38:39]
	global_load_dwordx4 v[26:29], v168, s[38:39] offset:2048
	global_load_dwordx4 v[34:37], v168, s[40:41]
	global_load_dwordx4 v[22:25], v168, s[40:41] offset:2048
	s_waitcnt lgkmcnt(0)
	s_barrier
	v_mov_b32_e32 v10, 0
	s_add_i32 s48, s67, 0x2000
	s_add_i32 s49, s67, 0x2400
	s_mov_b32 s50, 0
	s_mov_b64 s[8:9], 0
	v_mov_b32_e32 v11, v10
	v_mov_b32_e32 v12, v10
	v_mov_b32_e32 v13, v10
	v_mov_b32_e32 v62, v10
	v_mov_b32_e32 v63, v10
	v_mov_b32_e32 v64, v10
	v_mov_b32_e32 v65, v10
	v_mov_b32_e32 v70, v10
	v_mov_b32_e32 v71, v10
	v_mov_b32_e32 v72, v10
	v_mov_b32_e32 v73, v10

.LBB0_869:
	s_sub_i32 s11, s62, s64
	v_mov_b32_e32 v162, v0
	s_min_i32 s11, s11, 0x200
	s_add_i32 s12, s11, 0x7f
	v_readfirstlane_b32 s10, v162
	s_lshr_b32 s66, s12, 7
	s_ashr_i32 s12, s10, 2
	s_and_b32 s12, s12, -16
	s_mul_i32 s12, s12, s66
	s_add_i32 s12, s12, s64
	v_bfe_u32 v2, v162, 3, 3
	v_or_b32_e32 v10, s12, v2
	s_add_i32 s65, s11, s64
	v_mov_b32_e32 v11, s64
	v_cmp_gt_i32_e32 vcc, s65, v10
	v_or_b32_e32 v4, 8, v10
	v_add_u32_e32 v6, 16, v10
	v_cndmask_b32_e32 v2, v11, v10, vcc
	v_cmp_gt_i32_e32 vcc, s65, v4
	s_cmpk_gt_u32 s11, 0x80
	s_cselect_b64 s[44:45], -1, 0
	v_cndmask_b32_e32 v4, v11, v4, vcc
	v_cmp_gt_i32_e32 vcc, s65, v6
	s_and_b64 vcc, s[44:45], vcc
	v_add_u32_e32 v8, 24, v10
	v_cndmask_b32_e32 v6, v11, v6, vcc
	v_cmp_gt_i32_e32 vcc, s65, v8
	s_and_b64 vcc, s[44:45], vcc
	v_ashrrev_i32_e32 v3, 31, v2
	v_ashrrev_i32_e32 v7, 31, v6
	v_cndmask_b32_e32 v8, v11, v8, vcc
	v_lshl_add_u64 v[2:3], v[2:3], 2, s[24:25]
	v_ashrrev_i32_e32 v5, 31, v4
	v_lshl_add_u64 v[6:7], v[6:7], 2, s[24:25]
	v_ashrrev_i32_e32 v9, 31, v8
	v_lshl_add_u64 v[4:5], v[4:5], 2, s[24:25]
	v_lshl_add_u64 v[8:9], v[8:9], 2, s[24:25]
	global_load_dword v12, v[2:3], off
	global_load_dword v13, v[4:5], off
	s_nop 0
	global_load_dword v6, v[6:7], off
	s_nop 0
	global_load_dword v7, v[8:9], off
	v_add_u32_e32 v2, 32, v10
	s_cmpk_gt_u32 s11, 0x100
	s_cselect_b64 s[42:43], -1, 0
	v_cmp_gt_i32_e32 vcc, s65, v2
	s_and_b64 vcc, s[42:43], vcc
	v_add_u32_e32 v4, 40, v10
	v_cndmask_b32_e32 v2, v11, v2, vcc
	v_cmp_gt_i32_e32 vcc, s65, v4
	s_and_b64 vcc, s[42:43], vcc
	v_ashrrev_i32_e32 v3, 31, v2
	v_cndmask_b32_e32 v4, v11, v4, vcc
	v_lshl_add_u64 v[2:3], v[2:3], 2, s[24:25]
	v_ashrrev_i32_e32 v5, 31, v4
	v_lshl_add_u64 v[4:5], v[4:5], 2, s[24:25]
	global_load_dword v8, v[2:3], off
	global_load_dword v9, v[4:5], off
	v_add_u32_e32 v2, 48, v10
	s_cmpk_gt_u32 s11, 0x180
	s_cselect_b64 s[40:41], -1, 0
	v_cmp_gt_i32_e32 vcc, s65, v2
	s_and_b64 vcc, s[40:41], vcc
	v_add_u32_e32 v4, 56, v10
	v_cndmask_b32_e32 v2, v11, v2, vcc
	v_cmp_gt_i32_e32 vcc, s65, v4
	s_and_b64 vcc, s[40:41], vcc
	v_ashrrev_i32_e32 v3, 31, v2
	v_cndmask_b32_e32 v4, v11, v4, vcc
	v_lshl_add_u64 v[2:3], v[2:3], 2, s[24:25]
	v_ashrrev_i32_e32 v5, 31, v4
	v_lshl_add_u64 v[4:5], v[4:5], 2, s[24:25]
	global_load_dword v131, v[2:3], off
	global_load_dword v130, v[4:5], off
	v_and_b32_e32 v10, 31, v162
	v_and_b32_e32 v2, 7, v162
	v_bfe_u32 v3, v162, 4, 2
	v_cmp_gt_u32_e32 vcc, 16, v10
	v_bitop3_b32 v2, v3, v2, 4 bitop3:0x36
	v_ashrrev_i32_e32 v11, 5, v162
	v_cndmask_b32_e32 v15, v166, v167, vcc
	v_bitop3_b32 v14, v3, v162, 7 bitop3:0x78
	v_lshlrev_b32_e32 v132, 4, v2
	v_lshl_add_u32 v2, v10, 4, v15
	v_lshlrev_b32_e32 v133, 4, v14
	v_lshl_or_b32 v168, v11, 13, v2
	global_load_dwordx4 v[228:231], v168, s[22:23]
	global_load_dwordx4 v[232:235], v168, s[22:23] offset:2048
	global_load_dwordx4 v[236:239], v168, s[28:29]
	global_load_dwordx4 v[240:243], v168, s[28:29] offset:2048
	global_load_dwordx4 v[60:63], v168, s[30:31]
	global_load_dwordx4 v[64:67], v168, s[30:31] offset:2048
	global_load_dwordx4 v[68:71], v168, s[34:35]
	global_load_dwordx4 v[72:75], v168, s[34:35] offset:2048
	v_lshrrev_b32_e32 v5, 4, v162
	v_lshlrev_b32_e32 v3, 11, v3
	s_lshl_b32 s10, s10, 8
	s_and_b32 s10, s10, 0xffffc000
	v_and_b32_e32 v4, 15, v162
	s_add_i32 s67, s10, 0
	s_add_i32 s68, s67, 0x400
	s_mov_b64 s[10:11], -1
	s_mov_b64 s[12:13], 0
	s_cmp_lt_i32 s66, 2
	s_mov_b64 s[14:15], 0
	s_waitcnt vmcnt(15)
	v_lshlrev_b32_e32 v2, 8, v12
	v_and_or_b32 v169, v2, s60, v133
	s_waitcnt vmcnt(14)
	v_lshlrev_b32_e32 v2, 8, v13
	v_and_or_b32 v170, v2, s60, v132
	s_waitcnt vmcnt(13)
	v_lshlrev_b32_e32 v2, 8, v6
	s_waitcnt vmcnt(12)
	v_lshlrev_b32_e32 v6, 8, v7
	v_and_or_b32 v175, v6, s60, v132
	v_and_or_b32 v174, v2, s60, v133
	s_waitcnt vmcnt(11)
	v_lshlrev_b32_e32 v2, 8, v8
	s_waitcnt vmcnt(10)
	v_lshlrev_b32_e32 v6, 8, v9
	v_and_or_b32 v177, v6, s60, v132
	v_lshlrev_b32_e32 v6, 3, v162
	v_and_or_b32 v176, v2, s60, v133
	v_lshlrev_b32_e32 v2, 10, v11
	v_and_b32_e32 v6, 24, v6
	v_add3_u32 v173, s61, v2, v6
	v_bfe_u32 v2, v162, 2, 3
	v_bitop3_b32 v134, v2, v5, 4 bitop3:0x78
	v_bfe_u32 v2, v162, 2, 2
	v_lshlrev_b32_e32 v7, 8, v2
	v_add3_u32 v3, s61, v3, v7
	v_lshrrev_b32_e32 v7, 2, v162
	v_and_or_b32 v2, v7, 4, v2
	v_lshlrev_b32_e32 v2, 5, v2
	v_add3_u32 v171, v3, v6, v2
	v_bfe_u32 v3, v162, 1, 3
	v_bitop3_b32 v3, v5, v3, 3 bitop3:0x6c
	v_lshlrev_b32_e32 v2, 7, v4
	v_lshlrev_b32_e32 v3, 4, v3
	v_add3_u32 v172, s67, v2, v3
	s_cbranch_scc1 .LBB0_881
	s_cmp_gt_i32 s66, 2
	s_cbranch_scc0 .LBB0_875
	s_cmp_eq_u32 s66, 3
	s_mov_b64 s[14:15], -1
	s_cbranch_scc0 .LBB0_876
	s_mov_b32 s10, m0
	s_mov_b32 m0, s67
	s_nop 0
	global_load_lds_dwordx4 v169, s[8:9]
	s_mov_b32 m0, s10
	s_add_i32 s50, s67, 0x800
	s_mov_b32 s10, m0
	s_mov_b32 m0, s68
	s_nop 0
	global_load_lds_dwordx4 v170, s[8:9]
	s_mov_b32 m0, s10
	s_add_i32 s51, s67, 0xc00
	s_mov_b32 s10, m0
	s_mov_b32 m0, s50
	s_nop 0
	global_load_lds_dwordx4 v174, s[8:9]
	s_mov_b32 m0, s10
	s_add_i32 s69, s67, 0x1000
	s_mov_b32 s10, m0
	s_mov_b32 m0, s51
	s_nop 0
	global_load_lds_dwordx4 v175, s[8:9]
	s_mov_b32 m0, s10
	s_add_i32 s70, s67, 0x1400
	s_mov_b32 s10, m0
	s_mov_b32 m0, s69
	s_nop 0
	global_load_lds_dwordx4 v176, s[8:9]
	s_mov_b32 m0, s10
	v_mov_b32_e32 v26, 0
	s_mov_b32 s10, m0
	s_mov_b32 m0, s70
	s_nop 0
	global_load_lds_dwordx4 v177, s[8:9]
	s_mov_b32 m0, s10
	v_mov_b32_e32 v27, 0
	v_mov_b32_e32 v28, 0
	v_mov_b32_e32 v29, 0
	v_mov_b32_e32 v10, 0
	v_mov_b32_e32 v11, 0
	v_mov_b32_e32 v12, 0
	v_mov_b32_e32 v13, 0
	v_mov_b32_e32 v50, 0
	v_mov_b32_e32 v51, 0
	v_mov_b32_e32 v52, 0
	v_mov_b32_e32 v53, 0
	v_mov_b32_e32 v14, 0
	v_mov_b32_e32 v15, 0
	v_mov_b32_e32 v16, 0
	v_mov_b32_e32 v17, 0
	v_mov_b32_e32 v30, 0
	v_mov_b32_e32 v31, 0
	v_mov_b32_e32 v32, 0
	v_mov_b32_e32 v33, 0
	v_mov_b32_e32 v34, 0
	v_mov_b32_e32 v35, 0
	v_mov_b32_e32 v36, 0
	v_mov_b32_e32 v37, 0
	v_mov_b32_e32 v82, 0
	v_mov_b32_e32 v83, 0
	v_mov_b32_e32 v84, 0
	v_mov_b32_e32 v85, 0
	v_mov_b32_e32 v54, 0
	v_mov_b32_e32 v55, 0
	v_mov_b32_e32 v56, 0
	v_mov_b32_e32 v57, 0
	v_mov_b32_e32 v86, 0
	v_mov_b32_e32 v87, 0
	v_mov_b32_e32 v88, 0
	v_mov_b32_e32 v89, 0
	v_mov_b32_e32 v22, 0
	v_mov_b32_e32 v23, 0
	v_mov_b32_e32 v24, 0
	v_mov_b32_e32 v25, 0
	v_mov_b32_e32 v6, 0
	v_mov_b32_e32 v7, 0
	v_mov_b32_e32 v8, 0
	v_mov_b32_e32 v9, 0
	v_mov_b32_e32 v42, 0
	v_mov_b32_e32 v43, 0
	v_mov_b32_e32 v44, 0
	v_mov_b32_e32 v45, 0
	v_mov_b32_e32 v38, 0
	v_mov_b32_e32 v39, 0
	v_mov_b32_e32 v40, 0
	v_mov_b32_e32 v41, 0
	v_mov_b32_e32 v18, 0
	v_mov_b32_e32 v19, 0
	v_mov_b32_e32 v20, 0
	v_mov_b32_e32 v21, 0
	v_mov_b32_e32 v58, 0
	v_mov_b32_e32 v59, 0
	v_mov_b32_e32 v46, 0
	v_mov_b32_e32 v47, 0
	v_mov_b32_e32 v48, 0
	v_mov_b32_e32 v49, 0
	v_mov_b32_e32 v90, 0
	v_mov_b32_e32 v91, 0
	v_mov_b32_e32 v92, 0
	v_mov_b32_e32 v93, 0
	v_mov_b32_e32 v78, 0
	v_mov_b32_e32 v79, 0
	v_mov_b32_e32 v80, 0
	v_mov_b32_e32 v81, 0
	v_mov_b32_e32 v76, 0
	v_mov_b32_e32 v77, 0
	v_mov_b32_e32 v94, 0
	v_mov_b32_e32 v95, 0
	v_mov_b32_e32 v96, 0
	v_mov_b32_e32 v97, 0
	s_waitcnt vmcnt(6)
	v_mov_b32_e32 v106, v60
	v_mov_b32_e32 v107, v61
	v_mov_b32_e32 v108, v62
	v_mov_b32_e32 v109, v63
	v_mov_b32_e32 v102, v64
	v_mov_b32_e32 v103, v65
	v_mov_b32_e32 v104, v66
	v_mov_b32_e32 v105, v67
	v_mov_b32_e32 v110, v68
	v_mov_b32_e32 v111, v69
	v_mov_b32_e32 v112, v70
	v_mov_b32_e32 v113, v71
	v_mov_b32_e32 v98, v72
	v_mov_b32_e32 v99, v73
	v_mov_b32_e32 v100, v74
	v_mov_b32_e32 v101, v75
	v_xor_b32_e32 v139, 64, v172
	v_cvt_pk_bf16_f32 v2, v228, v229
	v_cvt_pk_bf16_f32 v3, v230, v231
	v_lshlrev_b32_e32 v4, 5, v134
	v_add_u32_e32 v135, v173, v4
	v_xor_b32_e32 v5, 32, v4
	ds_write_b64 v135, v[2:3]
	v_cvt_pk_bf16_f32 v2, v232, v233
	v_cvt_pk_bf16_f32 v3, v234, v235
	v_add_u32_e32 v136, v173, v5
	v_xor_b32_e32 v5, 64, v4
	ds_write_b64 v136, v[2:3] offset:256
	v_cvt_pk_bf16_f32 v2, v236, v237
	v_cvt_pk_bf16_f32 v3, v238, v239
	v_add_u32_e32 v137, v173, v5
	v_xor_b32_e32 v4, 0x60, v4
	ds_write_b64 v137, v[2:3] offset:512
	v_cvt_pk_bf16_f32 v2, v240, v241
	v_cvt_pk_bf16_f32 v3, v242, v243
	v_add_u32_e32 v138, v173, v4
	ds_write_b64 v138, v[2:3] offset:768
	global_load_dwordx4 v[122:125], v168, s[36:37]
	global_load_dwordx4 v[118:121], v168, s[36:37] offset:2048
	global_load_dwordx4 v[126:129], v168, s[38:39]
	global_load_dwordx4 v[114:117], v168, s[38:39] offset:2048
	s_waitcnt lgkmcnt(0)
	s_barrier
	v_add_u32_e32 v2, 0x2000, v172
	s_add_i32 s71, s67, 0x2000
	v_xor_b32_e32 v140, 64, v2
	v_xor_b32_e32 v141, 32, v171
	v_xor_b32_e32 v142, 64, v171
	v_xor_b32_e32 v143, 0x60, v171
	v_xor_b32_e32 v144, 0x80, v171
	v_xor_b32_e32 v145, 0xa0, v171
	v_xor_b32_e32 v146, 0xc0, v171
	s_add_i32 s72, s67, 0x2400
	v_xor_b32_e32 v147, 0xe0, v171
	s_add_i32 s73, s67, 0x2800
	s_add_i32 s74, s67, 0x2c00
	s_add_i32 s75, s67, 0x3000
	s_add_i32 s76, s67, 0x3400
	s_mov_b32 s48, 0
	s_mov_b64 s[14:15], 0
	v_mov_b32_e32 v2, v26
	v_mov_b32_e32 v3, v26
	v_mov_b32_e32 v4, v26
	v_mov_b32_e32 v5, v26
	v_mov_b32_e32 v66, v26
	v_mov_b32_e32 v67, v26
	v_mov_b32_e32 v68, v26
	v_mov_b32_e32 v69, v26
	v_mov_b32_e32 v62, v26
	v_mov_b32_e32 v63, v26
	v_mov_b32_e32 v64, v26
	v_mov_b32_e32 v65, v26
	v_mov_b32_e32 v70, v26
	v_mov_b32_e32 v71, v26
	v_mov_b32_e32 v72, v26
	v_mov_b32_e32 v73, v26
	v_mov_b32_e32 v60, v26
	v_mov_b32_e32 v61, v26
	v_mov_b32_e32 v74, v26
	v_mov_b32_e32 v75, v26

.LBB0_877:
	s_mov_b32 s10, m0
	s_mov_b32 m0, s67
	s_nop 0
	global_load_lds_dwordx4 v169, s[8:9]
	s_mov_b32 m0, s10
	s_add_i32 s69, s67, 0x800
	s_mov_b32 s10, m0
	s_mov_b32 m0, s68
	s_nop 0
	global_load_lds_dwordx4 v170, s[8:9]
	s_mov_b32 m0, s10
	s_add_i32 s70, s67, 0xc00
	s_mov_b32 s10, m0
	s_mov_b32 m0, s69
	s_nop 0
	global_load_lds_dwordx4 v174, s[8:9]
	s_mov_b32 m0, s10
	v_xor_b32_e32 v102, 64, v172
	s_mov_b32 s10, m0
	s_mov_b32 m0, s70
	s_nop 0
	global_load_lds_dwordx4 v175, s[8:9]
	s_mov_b32 m0, s10
	v_mov_b32_e32 v10, 0
	v_mov_b32_e32 v11, 0
	v_mov_b32_e32 v12, 0
	v_mov_b32_e32 v13, 0
	v_mov_b32_e32 v14, 0
	v_mov_b32_e32 v15, 0
	v_mov_b32_e32 v16, 0
	v_mov_b32_e32 v17, 0
	v_mov_b32_e32 v30, 0
	v_mov_b32_e32 v31, 0
	v_mov_b32_e32 v32, 0
	v_mov_b32_e32 v33, 0
	v_mov_b32_e32 v34, 0
	v_mov_b32_e32 v35, 0
	v_mov_b32_e32 v36, 0
	v_mov_b32_e32 v37, 0
	v_mov_b32_e32 v54, 0
	v_mov_b32_e32 v55, 0
	v_mov_b32_e32 v56, 0
	v_mov_b32_e32 v57, 0
	v_mov_b32_e32 v86, 0
	v_mov_b32_e32 v87, 0
	v_mov_b32_e32 v88, 0
	v_mov_b32_e32 v89, 0
	v_mov_b32_e32 v6, 0
	v_mov_b32_e32 v7, 0
	v_mov_b32_e32 v8, 0
	v_mov_b32_e32 v9, 0
	v_mov_b32_e32 v42, 0
	v_mov_b32_e32 v43, 0
	v_mov_b32_e32 v44, 0
	v_mov_b32_e32 v45, 0
	v_mov_b32_e32 v18, 0
	v_mov_b32_e32 v19, 0
	v_mov_b32_e32 v20, 0
	v_mov_b32_e32 v21, 0
	v_mov_b32_e32 v46, 0
	v_mov_b32_e32 v47, 0
	v_mov_b32_e32 v48, 0
	v_mov_b32_e32 v49, 0
	v_mov_b32_e32 v90, 0
	v_mov_b32_e32 v91, 0
	v_mov_b32_e32 v92, 0
	v_mov_b32_e32 v93, 0
	v_mov_b32_e32 v76, 0
	v_mov_b32_e32 v77, 0
	v_mov_b32_e32 v94, 0
	v_mov_b32_e32 v95, 0
	v_mov_b32_e32 v96, 0
	v_mov_b32_e32 v97, 0
	s_waitcnt vmcnt(4)
	v_mov_b32_e32 v38, v60
	v_mov_b32_e32 v39, v61
	v_mov_b32_e32 v40, v62
	v_mov_b32_e32 v41, v63
	v_mov_b32_e32 v26, v64
	v_mov_b32_e32 v27, v65
	v_mov_b32_e32 v28, v66
	v_mov_b32_e32 v29, v67
	v_mov_b32_e32 v50, v68
	v_mov_b32_e32 v51, v69
	v_mov_b32_e32 v52, v70
	v_mov_b32_e32 v53, v71
	v_mov_b32_e32 v22, v72
	v_mov_b32_e32 v23, v73
	v_mov_b32_e32 v24, v74
	v_mov_b32_e32 v25, v75
	s_add_i32 s71, s67, 0x2000
	v_cvt_pk_bf16_f32 v2, v228, v229
	v_cvt_pk_bf16_f32 v3, v230, v231
	v_lshlrev_b32_e32 v4, 5, v134
	v_add_u32_e32 v98, v173, v4
	v_xor_b32_e32 v5, 32, v4
	ds_write_b64 v98, v[2:3]
	v_cvt_pk_bf16_f32 v2, v232, v233
	v_cvt_pk_bf16_f32 v3, v234, v235
	v_add_u32_e32 v99, v173, v5
	v_xor_b32_e32 v5, 64, v4
	ds_write_b64 v99, v[2:3] offset:256
	v_cvt_pk_bf16_f32 v2, v236, v237
	v_cvt_pk_bf16_f32 v3, v238, v239
	v_add_u32_e32 v100, v173, v5
	v_xor_b32_e32 v4, 0x60, v4
	ds_write_b64 v100, v[2:3] offset:512
	v_cvt_pk_bf16_f32 v2, v240, v241
	v_cvt_pk_bf16_f32 v3, v242, v243
	v_add_u32_e32 v101, v173, v4
	ds_write_b64 v101, v[2:3] offset:768
	global_load_dwordx4 v[78:81], v168, s[36:37]
	global_load_dwordx4 v[66:69], v168, s[36:37] offset:2048
	global_load_dwordx4 v[82:85], v168, s[38:39]
	global_load_dwordx4 v[58:61], v168, s[38:39] offset:2048
	s_waitcnt lgkmcnt(0)
	s_barrier
	v_add_u32_e32 v2, 0x2000, v172
	v_xor_b32_e32 v103, 64, v2
	v_mov_b32_e32 v2, 0
	v_xor_b32_e32 v104, 32, v171
	v_xor_b32_e32 v105, 64, v171
	v_xor_b32_e32 v106, 0x60, v171
	v_xor_b32_e32 v107, 0x80, v171
	v_xor_b32_e32 v108, 0xa0, v171
	v_xor_b32_e32 v109, 0xc0, v171
	s_add_i32 s72, s67, 0x2400
	v_xor_b32_e32 v110, 0xe0, v171
	s_add_i32 s73, s67, 0x2800
	s_add_i32 s74, s67, 0x2c00
	s_mov_b32 s50, 0
	s_mov_b64 s[46:47], 0
	v_mov_b32_e32 v3, v2
	v_mov_b32_e32 v4, v2
	v_mov_b32_e32 v5, v2
	v_mov_b32_e32 v62, v2
	v_mov_b32_e32 v63, v2
	v_mov_b32_e32 v64, v2
	v_mov_b32_e32 v65, v2
	v_mov_b32_e32 v70, v2
	v_mov_b32_e32 v71, v2
	v_mov_b32_e32 v72, v2
	v_mov_b32_e32 v73, v2
	v_mov_b32_e32 v74, v2
	v_mov_b32_e32 v75, v2

.LBB0_883:
	v_mov_b32_e32 v125, 0
	v_lshlrev_b32_e32 v98, 5, v134
	v_add_u32_e32 v99, 0x2000, v172
	s_andn2_b64 vcc, exec, s[14:15]
	v_xor_b32_e32 v178, 64, v172
	v_xor_b32_e32 v179, 32, v171
	v_xor_b32_e32 v180, 64, v171
	v_xor_b32_e32 v181, 0x60, v171
	v_xor_b32_e32 v182, 0x80, v171
	v_xor_b32_e32 v183, 0xa0, v171
	v_xor_b32_e32 v184, 0xc0, v171
	v_xor_b32_e32 v185, 0xe0, v171
	v_add_u32_e32 v186, v173, v98
	v_xor_b32_e32 v190, 32, v98
	v_xor_b32_e32 v189, 64, v98
	v_xor_b32_e32 v188, 0x60, v98
	v_xor_b32_e32 v187, 64, v99
	v_mov_b32_e32 v124, v125
	v_mov_b32_e32 v123, v125
	v_mov_b32_e32 v122, v125
	v_mov_b32_e32 v117, v125
	v_mov_b32_e32 v116, v125
	v_mov_b32_e32 v115, v125
	v_mov_b32_e32 v114, v125
	v_mov_b32_e32 v109, v125
	v_mov_b32_e32 v108, v125
	v_mov_b32_e32 v107, v125
	v_mov_b32_e32 v106, v125
	v_mov_b32_e32 v105, v125
	v_mov_b32_e32 v104, v125
	v_mov_b32_e32 v103, v125
	v_mov_b32_e32 v102, v125
	v_mov_b32_e32 v129, v125
	v_mov_b32_e32 v128, v125
	v_mov_b32_e32 v127, v125
	v_mov_b32_e32 v126, v125
	v_mov_b32_e32 v121, v125
	v_mov_b32_e32 v120, v125
	v_mov_b32_e32 v119, v125
	v_mov_b32_e32 v118, v125
	v_mov_b32_e32 v113, v125
	v_mov_b32_e32 v112, v125
	v_mov_b32_e32 v111, v125
	v_mov_b32_e32 v110, v125
	v_mov_b32_e32 v101, v125
	v_mov_b32_e32 v100, v125
	v_mov_b32_e32 v99, v125
	v_mov_b32_e32 v98, v125
	s_cbranch_vccnz .LBB0_887
	s_waitcnt vmcnt(9)
	v_lshlrev_b32_e32 v2, 8, v131
	v_and_or_b32 v191, v2, s60, v133
	s_waitcnt vmcnt(8)
	v_lshlrev_b32_e32 v2, 8, v130
	v_and_or_b32 v192, v2, s60, v132
	s_mov_b32 s10, m0
	s_mov_b32 m0, s67
	s_nop 0
	global_load_lds_dwordx4 v169, s[8:9]
	s_mov_b32 m0, s10
	s_add_i32 s48, s67, 0x800
	s_mov_b32 s10, m0
	s_mov_b32 m0, s68
	s_nop 0
	global_load_lds_dwordx4 v170, s[8:9]
	s_mov_b32 m0, s10
	s_add_i32 s49, s67, 0xc00
	s_mov_b32 s10, m0
	s_mov_b32 m0, s48
	s_nop 0
	global_load_lds_dwordx4 v174, s[8:9]
	s_mov_b32 m0, s10
	s_add_i32 s50, s67, 0x1000
	s_mov_b32 s10, m0
	s_mov_b32 m0, s49
	s_nop 0
	global_load_lds_dwordx4 v175, s[8:9]
	s_mov_b32 m0, s10
	s_add_i32 s51, s67, 0x1400
	s_mov_b32 s10, m0
	s_mov_b32 m0, s50
	s_nop 0
	global_load_lds_dwordx4 v176, s[8:9]
	s_mov_b32 m0, s10
	s_add_i32 s69, s67, 0x1800
	s_mov_b32 s10, m0
	s_mov_b32 m0, s51
	s_nop 0
	global_load_lds_dwordx4 v177, s[8:9]
	s_mov_b32 m0, s10
	s_add_i32 s70, s67, 0x1c00
	s_mov_b32 s10, m0
	s_mov_b32 m0, s69
	s_nop 0
	global_load_lds_dwordx4 v191, s[8:9]
	s_mov_b32 m0, s10
	v_add_u32_e32 v193, v173, v190
	s_mov_b32 s10, m0
	s_mov_b32 m0, s70
	s_nop 0
	global_load_lds_dwordx4 v192, s[8:9]
	s_mov_b32 m0, s10
	v_mov_b32_e32 v99, 0
	v_mov_b32_e32 v100, 0
	v_mov_b32_e32 v101, 0
	v_mov_b32_e32 v26, 0
	v_mov_b32_e32 v27, 0
	v_mov_b32_e32 v28, 0
	v_mov_b32_e32 v29, 0
	v_mov_b32_e32 v4, 0
	v_mov_b32_e32 v5, 0
	v_mov_b32_e32 v10, 0
	v_mov_b32_e32 v11, 0
	v_mov_b32_e32 v12, 0
	v_mov_b32_e32 v13, 0
	v_mov_b32_e32 v110, 0
	v_mov_b32_e32 v111, 0
	v_mov_b32_e32 v112, 0
	v_mov_b32_e32 v113, 0
	v_mov_b32_e32 v50, 0
	v_mov_b32_e32 v51, 0
	v_mov_b32_e32 v52, 0
	v_mov_b32_e32 v53, 0
	v_mov_b32_e32 v14, 0
	v_mov_b32_e32 v15, 0
	v_mov_b32_e32 v16, 0
	v_mov_b32_e32 v17, 0
	v_mov_b32_e32 v30, 0
	v_mov_b32_e32 v31, 0
	v_mov_b32_e32 v32, 0
	v_mov_b32_e32 v33, 0
	v_mov_b32_e32 v118, 0
	v_mov_b32_e32 v119, 0
	v_mov_b32_e32 v120, 0
	v_mov_b32_e32 v121, 0
	v_mov_b32_e32 v34, 0
	v_mov_b32_e32 v35, 0
	v_mov_b32_e32 v36, 0
	v_mov_b32_e32 v37, 0
	v_mov_b32_e32 v126, 0
	v_mov_b32_e32 v127, 0
	v_mov_b32_e32 v128, 0
	v_mov_b32_e32 v129, 0
	v_mov_b32_e32 v82, 0
	v_mov_b32_e32 v83, 0
	v_mov_b32_e32 v84, 0
	v_mov_b32_e32 v85, 0
	v_mov_b32_e32 v54, 0
	v_mov_b32_e32 v55, 0
	v_mov_b32_e32 v56, 0
	v_mov_b32_e32 v57, 0
	v_mov_b32_e32 v86, 0
	v_mov_b32_e32 v87, 0
	v_mov_b32_e32 v88, 0
	v_mov_b32_e32 v89, 0
	v_mov_b32_e32 v102, 0
	v_mov_b32_e32 v103, 0
	v_mov_b32_e32 v104, 0
	v_mov_b32_e32 v105, 0
	v_mov_b32_e32 v22, 0
	v_mov_b32_e32 v23, 0
	v_mov_b32_e32 v24, 0
	v_mov_b32_e32 v25, 0
	v_mov_b32_e32 v6, 0
	v_mov_b32_e32 v7, 0
	v_mov_b32_e32 v8, 0
	v_mov_b32_e32 v9, 0
	v_mov_b32_e32 v42, 0
	v_mov_b32_e32 v43, 0
	v_mov_b32_e32 v44, 0
	v_mov_b32_e32 v45, 0
	v_mov_b32_e32 v106, 0
	v_mov_b32_e32 v107, 0
	v_mov_b32_e32 v108, 0
	v_mov_b32_e32 v109, 0
	v_mov_b32_e32 v38, 0
	v_mov_b32_e32 v39, 0
	v_mov_b32_e32 v40, 0
	v_mov_b32_e32 v41, 0
	v_mov_b32_e32 v18, 0
	v_mov_b32_e32 v19, 0
	v_mov_b32_e32 v20, 0
	v_mov_b32_e32 v21, 0
	v_mov_b32_e32 v114, 0
	v_mov_b32_e32 v115, 0
	v_mov_b32_e32 v116, 0
	v_mov_b32_e32 v117, 0
	v_mov_b32_e32 v58, 0
	v_mov_b32_e32 v59, 0
	v_mov_b32_e32 v46, 0
	v_mov_b32_e32 v47, 0
	v_mov_b32_e32 v48, 0
	v_mov_b32_e32 v49, 0
	v_mov_b32_e32 v90, 0
	v_mov_b32_e32 v91, 0
	v_mov_b32_e32 v92, 0
	v_mov_b32_e32 v93, 0
	v_mov_b32_e32 v122, 0
	v_mov_b32_e32 v123, 0
	v_mov_b32_e32 v124, 0
	v_mov_b32_e32 v125, 0
	v_mov_b32_e32 v78, 0
	v_mov_b32_e32 v79, 0
	v_mov_b32_e32 v80, 0
	v_mov_b32_e32 v81, 0
	v_mov_b32_e32 v76, 0
	v_mov_b32_e32 v77, 0
	v_mov_b32_e32 v94, 0
	v_mov_b32_e32 v95, 0
	v_mov_b32_e32 v96, 0
	v_mov_b32_e32 v97, 0
	s_waitcnt vmcnt(8)
	v_mov_b32_e32 v138, v60
	v_mov_b32_e32 v139, v61
	v_mov_b32_e32 v140, v62
	v_mov_b32_e32 v141, v63
	v_mov_b32_e32 v134, v64
	v_mov_b32_e32 v135, v65
	v_mov_b32_e32 v136, v66
	v_mov_b32_e32 v137, v67
	v_mov_b32_e32 v142, v68
	v_mov_b32_e32 v143, v69
	v_mov_b32_e32 v144, v70
	v_mov_b32_e32 v145, v71
	v_mov_b32_e32 v130, v72
	v_mov_b32_e32 v131, v73
	v_mov_b32_e32 v132, v74
	v_mov_b32_e32 v133, v75
	v_add_u32_e32 v194, v173, v189
	v_cvt_pk_bf16_f32 v2, v228, v229
	v_cvt_pk_bf16_f32 v3, v230, v231
	ds_write_b64 v186, v[2:3]
	v_cvt_pk_bf16_f32 v2, v232, v233
	v_cvt_pk_bf16_f32 v3, v234, v235
	ds_write_b64 v193, v[2:3] offset:256
	v_cvt_pk_bf16_f32 v2, v236, v237
	v_cvt_pk_bf16_f32 v3, v238, v239
	ds_write_b64 v194, v[2:3] offset:512
	v_cvt_pk_bf16_f32 v2, v240, v241
	v_cvt_pk_bf16_f32 v3, v242, v243
	v_add_u32_e32 v195, v173, v188
	ds_write_b64 v195, v[2:3] offset:768
	global_load_dwordx4 v[154:157], v168, s[36:37]
	global_load_dwordx4 v[150:153], v168, s[36:37] offset:2048
	global_load_dwordx4 v[158:161], v168, s[38:39]
	global_load_dwordx4 v[146:149], v168, s[38:39] offset:2048
	s_waitcnt lgkmcnt(0)
	s_barrier
	v_mov_b32_e32 v98, 0
	s_add_i32 s71, s67, 0x2000
	s_add_i32 s72, s67, 0x2400
	s_add_i32 s73, s67, 0x2800
	s_add_i32 s74, s67, 0x2c00
	s_add_i32 s75, s67, 0x3000
	s_add_i32 s76, s67, 0x3400
	s_add_i32 s77, s67, 0x3800
	s_add_i32 s78, s67, 0x3c00
	s_mov_b32 s46, 0
	s_mov_b64 s[12:13], 0
	v_mov_b32_e32 v2, v98
	v_mov_b32_e32 v3, v98
	v_mov_b32_e32 v66, v98
	v_mov_b32_e32 v67, v98
	v_mov_b32_e32 v68, v98
	v_mov_b32_e32 v69, v98
	v_mov_b32_e32 v62, v98
	v_mov_b32_e32 v63, v98
	v_mov_b32_e32 v64, v98
	v_mov_b32_e32 v65, v98
	v_mov_b32_e32 v70, v98
	v_mov_b32_e32 v71, v98
	v_mov_b32_e32 v72, v98
	v_mov_b32_e32 v73, v98
	v_mov_b32_e32 v60, v98
	v_mov_b32_e32 v61, v98
	v_mov_b32_e32 v74, v98
	v_mov_b32_e32 v75, v98

.LBB0_887:
	s_and_b64 vcc, exec, s[12:13]
	s_cbranch_vccz .LBB0_891
	s_mov_b32 s10, m0
	s_mov_b32 m0, s67
	s_nop 0
	global_load_lds_dwordx4 v169, s[8:9]
	s_mov_b32 m0, s10
	v_add_u32_e32 v47, v173, v189
	s_mov_b32 s10, m0
	s_mov_b32 m0, s68
	s_nop 0
	global_load_lds_dwordx4 v170, s[8:9]
	s_mov_b32 m0, s10
	v_mov_b32_e32 v30, 0
	v_mov_b32_e32 v31, 0
	v_mov_b32_e32 v32, 0
	v_mov_b32_e32 v33, 0
	v_mov_b32_e32 v86, 0
	v_mov_b32_e32 v87, 0
	v_mov_b32_e32 v88, 0
	v_mov_b32_e32 v89, 0
	v_mov_b32_e32 v42, 0
	v_mov_b32_e32 v43, 0
	v_mov_b32_e32 v44, 0
	v_mov_b32_e32 v45, 0
	v_mov_b32_e32 v90, 0
	v_mov_b32_e32 v91, 0
	v_mov_b32_e32 v92, 0
	v_mov_b32_e32 v93, 0
	v_mov_b32_e32 v94, 0
	v_mov_b32_e32 v95, 0
	v_mov_b32_e32 v96, 0
	v_mov_b32_e32 v97, 0
	s_waitcnt vmcnt(2)
	v_mov_b32_e32 v18, v60
	v_mov_b32_e32 v19, v61
	v_mov_b32_e32 v20, v62
	v_mov_b32_e32 v21, v63
	v_mov_b32_e32 v6, v64
	v_mov_b32_e32 v7, v65
	v_mov_b32_e32 v8, v66
	v_mov_b32_e32 v9, v67
	v_mov_b32_e32 v14, v68
	v_mov_b32_e32 v15, v69
	v_mov_b32_e32 v16, v70
	v_mov_b32_e32 v17, v71
	v_mov_b32_e32 v2, v72
	v_mov_b32_e32 v3, v73
	v_mov_b32_e32 v4, v74
	v_mov_b32_e32 v5, v75
	v_add_u32_e32 v46, v173, v190
	v_cvt_pk_bf16_f32 v10, v228, v229
	v_cvt_pk_bf16_f32 v11, v230, v231
	ds_write_b64 v186, v[10:11]
	v_cvt_pk_bf16_f32 v10, v236, v237
	v_cvt_pk_bf16_f32 v11, v238, v239
	v_cvt_pk_bf16_f32 v12, v232, v233
	v_cvt_pk_bf16_f32 v13, v234, v235
	ds_write_b64 v47, v[10:11] offset:512
	v_cvt_pk_bf16_f32 v10, v240, v241
	v_cvt_pk_bf16_f32 v11, v242, v243
	v_add_u32_e32 v48, v173, v188
	ds_write_b64 v46, v[12:13] offset:256
	ds_write_b64 v48, v[10:11] offset:768
	global_load_dwordx4 v[38:41], v168, s[36:37]
	global_load_dwordx4 v[26:29], v168, s[36:37] offset:2048
	global_load_dwordx4 v[34:37], v168, s[38:39]
	global_load_dwordx4 v[22:25], v168, s[38:39] offset:2048
	s_waitcnt lgkmcnt(0)
	s_barrier
	v_mov_b32_e32 v10, 0
	s_add_i32 s46, s67, 0x2000
	s_add_i32 s47, s67, 0x2400
	s_mov_b32 s48, 0
	s_mov_b64 s[12:13], 0
	v_mov_b32_e32 v11, v10
	v_mov_b32_e32 v12, v10
	v_mov_b32_e32 v13, v10
	v_mov_b32_e32 v62, v10
	v_mov_b32_e32 v63, v10
	v_mov_b32_e32 v64, v10
	v_mov_b32_e32 v65, v10
	v_mov_b32_e32 v70, v10
	v_mov_b32_e32 v71, v10
	v_mov_b32_e32 v72, v10
	v_mov_b32_e32 v73, v10
